# speedup vs baseline: 1.0200x; 1.0200x over previous
_Z7gemm128ILi3ELi96EEv8GemmArgs:
	s_cmp_ge_u32 s2, 0x100
	s_cbranch_scc1 .Ldn_exit
	s_load_dwordx4 s[4:7], s[0:1], 0x0
	s_load_dwordx2 s[8:9], s[0:1], 0x20
	s_load_dwordx2 s[10:11], s[0:1], 0x38
	s_and_b32 s12, s2, 7
	s_lshr_b32 s13, s2, 3
	s_lshl_b32 s12, s12, 5
	s_add_u32 s12, s12, s13
	s_and_b32 s13, s12, 3
	s_lshr_b32 s12, s12, 2
	s_lshl_b32 s12, s12, 7
	s_mul_i32 s13, s13, 0xc0
	v_lshrrev_b32_e32 v1, 6, v0
	v_and_b32_e32 v14, 7, v0
	v_bfe_u32 v15, v0, 4, 3
	v_xor_b32_e32 v14, v14, v15
	v_readfirstlane_b32 s14, v1
	v_lshrrev_b32_e32 v15, 3, v0
	v_mul_u32_u24_e32 v15, 0x1800, v15
	v_lshl_add_u32 v2, v14, 4, v15
	s_mov_b32 s22, 0x30000
	v_add_u32_e32 v3, s22, v2
	v_add_u32_e32 v4, s22, v3
	v_add_u32_e32 v5, s22, v4
	v_add_u32_e32 v6, s22, v5
	v_add_u32_e32 v7, s22, v6
	v_and_b32_e32 v14, 15, v0
	v_bfe_u32 v15, v0, 4, 2
	v_lshrrev_b32_e32 v16, 1, v14
	v_xor_b32_e32 v16, v16, v15
	v_lshlrev_b32_e32 v16, 4, v16
	v_bfe_u32 v17, v0, 7, 1
	v_bfe_u32 v18, v0, 6, 1
	v_lshl_add_u32 v19, v17, 6, v14
	v_lshl_add_u32 v8, v19, 7, v16
	v_mul_u32_u24_e32 v19, 0x60, v18
	v_add_u32_e32 v19, v19, v14
	v_lshl_add_u32 v9, v19, 7, v16
	v_add_u32_e32 v9, 0x4000, v9
	v_lshl_add_u32 v19, v17, 6, v14
	v_add_u32_e32 v19, s12, v19
	v_mul_u32_u24_e32 v19, 0xc00, v19
	v_mul_u32_u24_e32 v60, 0x60, v18
	v_lshl_add_u32 v60, v15, 2, v60
	v_add_u32_e32 v60, s13, v60
	v_lshl_add_u32 v56, v60, 2, v19
	s_mov_b32 s22, 0xc000
	v_add_u32_e32 v57, s22, v56
	v_add_u32_e32 v58, s22, v57
	v_add_u32_e32 v59, s22, v58
	s_waitcnt lgkmcnt(0)
	s_mul_i32 s22, s12, 0x1800
	s_add_u32 s16, s4, s22
	s_addc_u32 s17, s5, 0
	s_mul_i32 s22, s13, 0x1800
	s_add_u32 s18, s6, s22
	s_addc_u32 s19, s7, 0
	s_lshl_b32 s20, s14, 10
	s_mov_b32 s21, 0
	s_add_u32 m0, s20, 0x0
	s_nop 0
	global_load_lds_dwordx4 v2, s[16:17]
	s_add_u32 m0, s20, 0x1000
	s_nop 0
	global_load_lds_dwordx4 v3, s[16:17]
	s_add_u32 m0, s20, 0x2000
	s_nop 0
	global_load_lds_dwordx4 v4, s[16:17]
	s_add_u32 m0, s20, 0x3000
	s_nop 0
	global_load_lds_dwordx4 v5, s[16:17]
	s_add_u32 m0, s20, 0x4000
	s_nop 0
	global_load_lds_dwordx4 v2, s[18:19]
	s_add_u32 m0, s20, 0x5000
	s_nop 0
	global_load_lds_dwordx4 v3, s[18:19]
	s_add_u32 m0, s20, 0x6000
	s_nop 0
	global_load_lds_dwordx4 v4, s[18:19]
	s_add_u32 m0, s20, 0x7000
	s_nop 0
	global_load_lds_dwordx4 v5, s[18:19]
	s_add_u32 m0, s20, 0x8000
	s_nop 0
	global_load_lds_dwordx4 v6, s[18:19]
	s_add_u32 m0, s20, 0x9000
	s_nop 0
	global_load_lds_dwordx4 v7, s[18:19]
	s_add_u32 s16, s16, 0x80
	s_addc_u32 s17, s17, 0
	s_add_u32 s18, s18, 0x80
	s_addc_u32 s19, s19, 0
	s_add_u32 s20, s20, 0xa000
	s_cmp_ge_u32 s20, 0x1e000
	s_cbranch_scc0 .Ldn_ring_1
	s_sub_u32 s20, s20, 0x1e000
.Ldn_ring_1:
	s_add_u32 m0, s20, 0x0
	s_nop 0
	global_load_lds_dwordx4 v2, s[16:17]
	s_add_u32 m0, s20, 0x1000
	s_nop 0
	global_load_lds_dwordx4 v3, s[16:17]
	s_add_u32 m0, s20, 0x2000
	s_nop 0
	global_load_lds_dwordx4 v4, s[16:17]
	s_add_u32 m0, s20, 0x3000
	s_nop 0
	global_load_lds_dwordx4 v5, s[16:17]
	s_add_u32 m0, s20, 0x4000
	s_nop 0
	global_load_lds_dwordx4 v2, s[18:19]
	s_add_u32 m0, s20, 0x5000
	s_nop 0
	global_load_lds_dwordx4 v3, s[18:19]
	s_add_u32 m0, s20, 0x6000
	s_nop 0
	global_load_lds_dwordx4 v4, s[18:19]
	s_add_u32 m0, s20, 0x7000
	s_nop 0
	global_load_lds_dwordx4 v5, s[18:19]
	s_add_u32 m0, s20, 0x8000
	s_nop 0
	global_load_lds_dwordx4 v6, s[18:19]
	s_add_u32 m0, s20, 0x9000
	s_nop 0
	global_load_lds_dwordx4 v7, s[18:19]
	s_add_u32 s16, s16, 0x80
	s_addc_u32 s17, s17, 0
	s_add_u32 s18, s18, 0x80
	s_addc_u32 s19, s19, 0
	s_add_u32 s20, s20, 0xa000
	s_cmp_ge_u32 s20, 0x1e000
	s_cbranch_scc0 .Ldn_ring_2
	s_sub_u32 s20, s20, 0x1e000
.Ldn_ring_2:
	v_mov_b32_e32 v64, 0
	v_mov_b32_e32 v65, 0
	v_mov_b32_e32 v66, 0
	v_mov_b32_e32 v67, 0
	v_mov_b32_e32 v68, 0
	v_mov_b32_e32 v69, 0
	v_mov_b32_e32 v70, 0
	v_mov_b32_e32 v71, 0
	v_mov_b32_e32 v72, 0
	v_mov_b32_e32 v73, 0
	v_mov_b32_e32 v74, 0
	v_mov_b32_e32 v75, 0
	v_mov_b32_e32 v76, 0
	v_mov_b32_e32 v77, 0
	v_mov_b32_e32 v78, 0
	v_mov_b32_e32 v79, 0
	v_mov_b32_e32 v80, 0
	v_mov_b32_e32 v81, 0
	v_mov_b32_e32 v82, 0
	v_mov_b32_e32 v83, 0
	v_mov_b32_e32 v84, 0
	v_mov_b32_e32 v85, 0
	v_mov_b32_e32 v86, 0
	v_mov_b32_e32 v87, 0
	v_mov_b32_e32 v88, 0
	v_mov_b32_e32 v89, 0
	v_mov_b32_e32 v90, 0
	v_mov_b32_e32 v91, 0
	v_mov_b32_e32 v92, 0
	v_mov_b32_e32 v93, 0
	v_mov_b32_e32 v94, 0
	v_mov_b32_e32 v95, 0
	v_mov_b32_e32 v96, 0
	v_mov_b32_e32 v97, 0
	v_mov_b32_e32 v98, 0
	v_mov_b32_e32 v99, 0
	v_mov_b32_e32 v100, 0
	v_mov_b32_e32 v101, 0
	v_mov_b32_e32 v102, 0
	v_mov_b32_e32 v103, 0
	v_mov_b32_e32 v104, 0
	v_mov_b32_e32 v105, 0
	v_mov_b32_e32 v106, 0
	v_mov_b32_e32 v107, 0
	v_mov_b32_e32 v108, 0
	v_mov_b32_e32 v109, 0
	v_mov_b32_e32 v110, 0
	v_mov_b32_e32 v111, 0
	v_mov_b32_e32 v112, 0
	v_mov_b32_e32 v113, 0
	v_mov_b32_e32 v114, 0
	v_mov_b32_e32 v115, 0
	v_mov_b32_e32 v116, 0
	v_mov_b32_e32 v117, 0
	v_mov_b32_e32 v118, 0
	v_mov_b32_e32 v119, 0
	v_mov_b32_e32 v120, 0
	v_mov_b32_e32 v121, 0
	v_mov_b32_e32 v122, 0
	v_mov_b32_e32 v123, 0
	v_mov_b32_e32 v124, 0
	v_mov_b32_e32 v125, 0
	v_mov_b32_e32 v126, 0
	v_mov_b32_e32 v127, 0
	v_mov_b32_e32 v128, 0
	v_mov_b32_e32 v129, 0
	v_mov_b32_e32 v130, 0
	v_mov_b32_e32 v131, 0
	v_mov_b32_e32 v132, 0
	v_mov_b32_e32 v133, 0
	v_mov_b32_e32 v134, 0
	v_mov_b32_e32 v135, 0
	v_mov_b32_e32 v136, 0
	v_mov_b32_e32 v137, 0
	v_mov_b32_e32 v138, 0
	v_mov_b32_e32 v139, 0
	v_mov_b32_e32 v140, 0
	v_mov_b32_e32 v141, 0
	v_mov_b32_e32 v142, 0
	v_mov_b32_e32 v143, 0
	v_mov_b32_e32 v144, 0
	v_mov_b32_e32 v145, 0
	v_mov_b32_e32 v146, 0
	v_mov_b32_e32 v147, 0
	v_mov_b32_e32 v148, 0
	v_mov_b32_e32 v149, 0
	v_mov_b32_e32 v150, 0
	v_mov_b32_e32 v151, 0
	v_mov_b32_e32 v152, 0
	v_mov_b32_e32 v153, 0
	v_mov_b32_e32 v154, 0
	v_mov_b32_e32 v155, 0
	v_mov_b32_e32 v156, 0
	v_mov_b32_e32 v157, 0
	v_mov_b32_e32 v158, 0
	v_mov_b32_e32 v159, 0
	s_waitcnt vmcnt(10)
	s_barrier
	v_add_u32_e32 v10, s21, v8
	v_add_u32_e32 v12, s21, v9
	v_xor_b32_e32 v11, 64, v10
	v_xor_b32_e32 v13, 64, v12
	s_add_u32 s21, s21, 0xa000
	s_cmp_ge_u32 s21, 0x1e000
	s_cbranch_scc0 .Ldn_ring_3
	s_sub_u32 s21, s21, 0x1e000
.Ldn_ring_3:
	ds_read_b128 v[160:163], v10 offset:0
	ds_read_b128 v[164:167], v10 offset:2048
	ds_read_b128 v[168:171], v10 offset:4096
	ds_read_b128 v[172:175], v10 offset:6144
	ds_read_b128 v[176:179], v12 offset:0
	ds_read_b128 v[180:183], v12 offset:2048
	ds_read_b128 v[184:187], v12 offset:4096
	ds_read_b128 v[188:191], v12 offset:6144
	ds_read_b128 v[192:195], v12 offset:8192
	ds_read_b128 v[196:199], v12 offset:10240
	ds_read_b128 v[200:203], v11 offset:0
	ds_read_b128 v[204:207], v11 offset:2048
	ds_read_b128 v[208:211], v11 offset:4096
	ds_read_b128 v[212:215], v11 offset:6144
	ds_read_b128 v[216:219], v13 offset:0
	ds_read_b128 v[220:223], v13 offset:2048
	ds_read_b128 v[224:227], v13 offset:4096
	ds_read_b128 v[228:231], v13 offset:6144
	ds_read_b128 v[232:235], v13 offset:8192
	ds_read_b128 v[236:239], v13 offset:10240
	s_mov_b32 s15, 0
.Ldn_loop:
	s_waitcnt lgkmcnt(10)
	v_mfma_f32_16x16x32_bf16 v[64:67], v[176:179], v[160:163], v[64:67]
	s_add_u32 m0, s20, 0x0
	v_mfma_f32_16x16x32_bf16 v[68:71], v[176:179], v[164:167], v[68:71]
	global_load_lds_dwordx4 v2, s[16:17]
	v_mfma_f32_16x16x32_bf16 v[72:75], v[176:179], v[168:171], v[72:75]
	s_add_u32 m0, s20, 0x1000
	v_mfma_f32_16x16x32_bf16 v[76:79], v[176:179], v[172:175], v[76:79]
	global_load_lds_dwordx4 v3, s[16:17]
	v_mfma_f32_16x16x32_bf16 v[80:83], v[180:183], v[160:163], v[80:83]
	s_add_u32 m0, s20, 0x2000
	v_mfma_f32_16x16x32_bf16 v[84:87], v[180:183], v[164:167], v[84:87]
	global_load_lds_dwordx4 v4, s[16:17]
	v_mfma_f32_16x16x32_bf16 v[88:91], v[180:183], v[168:171], v[88:91]
	s_add_u32 m0, s20, 0x3000
	v_mfma_f32_16x16x32_bf16 v[92:95], v[180:183], v[172:175], v[92:95]
	global_load_lds_dwordx4 v5, s[16:17]
	v_mfma_f32_16x16x32_bf16 v[96:99], v[184:187], v[160:163], v[96:99]
	s_add_u32 m0, s20, 0x4000
	v_mfma_f32_16x16x32_bf16 v[100:103], v[184:187], v[164:167], v[100:103]
	global_load_lds_dwordx4 v2, s[18:19]
	v_mfma_f32_16x16x32_bf16 v[104:107], v[184:187], v[168:171], v[104:107]
	s_add_u32 m0, s20, 0x5000
	v_mfma_f32_16x16x32_bf16 v[108:111], v[184:187], v[172:175], v[108:111]
	global_load_lds_dwordx4 v3, s[18:19]
	v_mfma_f32_16x16x32_bf16 v[112:115], v[188:191], v[160:163], v[112:115]
	s_add_u32 m0, s20, 0x6000
	v_mfma_f32_16x16x32_bf16 v[116:119], v[188:191], v[164:167], v[116:119]
	global_load_lds_dwordx4 v4, s[18:19]
	v_mfma_f32_16x16x32_bf16 v[120:123], v[188:191], v[168:171], v[120:123]
	s_add_u32 m0, s20, 0x7000
	v_mfma_f32_16x16x32_bf16 v[124:127], v[188:191], v[172:175], v[124:127]
	global_load_lds_dwordx4 v5, s[18:19]
	v_mfma_f32_16x16x32_bf16 v[128:131], v[192:195], v[160:163], v[128:131]
	s_add_u32 m0, s20, 0x8000
	v_mfma_f32_16x16x32_bf16 v[132:135], v[192:195], v[164:167], v[132:135]
	global_load_lds_dwordx4 v6, s[18:19]
	v_mfma_f32_16x16x32_bf16 v[136:139], v[192:195], v[168:171], v[136:139]
	s_add_u32 m0, s20, 0x9000
	v_mfma_f32_16x16x32_bf16 v[140:143], v[192:195], v[172:175], v[140:143]
	global_load_lds_dwordx4 v7, s[18:19]
	v_mfma_f32_16x16x32_bf16 v[144:147], v[196:199], v[160:163], v[144:147]
	v_mfma_f32_16x16x32_bf16 v[148:151], v[196:199], v[164:167], v[148:151]
	v_mfma_f32_16x16x32_bf16 v[152:155], v[196:199], v[168:171], v[152:155]
	v_mfma_f32_16x16x32_bf16 v[156:159], v[196:199], v[172:175], v[156:159]
	s_add_u32 s16, s16, 0x80
	s_addc_u32 s17, s17, 0
	s_add_u32 s18, s18, 0x80
	s_addc_u32 s19, s19, 0
	s_add_u32 s20, s20, 0xa000
	s_cmp_ge_u32 s20, 0x1e000
	s_cbranch_scc0 .Ldn_ring_4
	s_sub_u32 s20, s20, 0x1e000
.Ldn_ring_4:
	s_waitcnt vmcnt(10) lgkmcnt(0)
	s_barrier
	v_add_u32_e32 v10, s21, v8
	v_add_u32_e32 v12, s21, v9
	v_xor_b32_e32 v11, 64, v10
	v_xor_b32_e32 v13, 64, v12
	s_add_u32 s21, s21, 0xa000
	s_cmp_ge_u32 s21, 0x1e000
	s_cbranch_scc0 .Ldn_ring_5
	s_sub_u32 s21, s21, 0x1e000
.Ldn_ring_5:
	v_mfma_f32_16x16x32_bf16 v[64:67], v[216:219], v[200:203], v[64:67]
	v_mfma_f32_16x16x32_bf16 v[68:71], v[216:219], v[204:207], v[68:71]
	ds_read_b128 v[160:163], v10 offset:0
	v_mfma_f32_16x16x32_bf16 v[72:75], v[216:219], v[208:211], v[72:75]
	v_mfma_f32_16x16x32_bf16 v[76:79], v[216:219], v[212:215], v[76:79]
	ds_read_b128 v[164:167], v10 offset:2048
	v_mfma_f32_16x16x32_bf16 v[80:83], v[220:223], v[200:203], v[80:83]
	v_mfma_f32_16x16x32_bf16 v[84:87], v[220:223], v[204:207], v[84:87]
	ds_read_b128 v[168:171], v10 offset:4096
	v_mfma_f32_16x16x32_bf16 v[88:91], v[220:223], v[208:211], v[88:91]
	v_mfma_f32_16x16x32_bf16 v[92:95], v[220:223], v[212:215], v[92:95]
	ds_read_b128 v[172:175], v10 offset:6144
	v_mfma_f32_16x16x32_bf16 v[96:99], v[224:227], v[200:203], v[96:99]
	v_mfma_f32_16x16x32_bf16 v[100:103], v[224:227], v[204:207], v[100:103]
	ds_read_b128 v[176:179], v12 offset:0
	v_mfma_f32_16x16x32_bf16 v[104:107], v[224:227], v[208:211], v[104:107]
	v_mfma_f32_16x16x32_bf16 v[108:111], v[224:227], v[212:215], v[108:111]
	ds_read_b128 v[180:183], v12 offset:2048
	v_mfma_f32_16x16x32_bf16 v[112:115], v[228:231], v[200:203], v[112:115]
	v_mfma_f32_16x16x32_bf16 v[116:119], v[228:231], v[204:207], v[116:119]
	ds_read_b128 v[184:187], v12 offset:4096
	v_mfma_f32_16x16x32_bf16 v[120:123], v[228:231], v[208:211], v[120:123]
	v_mfma_f32_16x16x32_bf16 v[124:127], v[228:231], v[212:215], v[124:127]
	ds_read_b128 v[188:191], v12 offset:6144
	v_mfma_f32_16x16x32_bf16 v[128:131], v[232:235], v[200:203], v[128:131]
	v_mfma_f32_16x16x32_bf16 v[132:135], v[232:235], v[204:207], v[132:135]
	ds_read_b128 v[192:195], v12 offset:8192
	v_mfma_f32_16x16x32_bf16 v[136:139], v[232:235], v[208:211], v[136:139]
	v_mfma_f32_16x16x32_bf16 v[140:143], v[232:235], v[212:215], v[140:143]
	ds_read_b128 v[196:199], v12 offset:10240
	v_mfma_f32_16x16x32_bf16 v[144:147], v[236:239], v[200:203], v[144:147]
	v_mfma_f32_16x16x32_bf16 v[148:151], v[236:239], v[204:207], v[148:151]
	v_mfma_f32_16x16x32_bf16 v[152:155], v[236:239], v[208:211], v[152:155]
	v_mfma_f32_16x16x32_bf16 v[156:159], v[236:239], v[212:215], v[156:159]
	ds_read_b128 v[200:203], v11 offset:0
	ds_read_b128 v[204:207], v11 offset:2048
	ds_read_b128 v[208:211], v11 offset:4096
	ds_read_b128 v[212:215], v11 offset:6144
	ds_read_b128 v[216:219], v13 offset:0
	ds_read_b128 v[220:223], v13 offset:2048
	ds_read_b128 v[224:227], v13 offset:4096
	ds_read_b128 v[228:231], v13 offset:6144
	ds_read_b128 v[232:235], v13 offset:8192
	ds_read_b128 v[236:239], v13 offset:10240
	s_add_u32 s15, s15, 1
	s_cmp_lt_u32 s15, 46
	s_cbranch_scc1 .Ldn_loop
	s_waitcnt lgkmcnt(10)
	v_mfma_f32_16x16x32_bf16 v[64:67], v[176:179], v[160:163], v[64:67]
	v_mfma_f32_16x16x32_bf16 v[68:71], v[176:179], v[164:167], v[68:71]
	v_mfma_f32_16x16x32_bf16 v[72:75], v[176:179], v[168:171], v[72:75]
	v_mfma_f32_16x16x32_bf16 v[76:79], v[176:179], v[172:175], v[76:79]
	v_mfma_f32_16x16x32_bf16 v[80:83], v[180:183], v[160:163], v[80:83]
	v_mfma_f32_16x16x32_bf16 v[84:87], v[180:183], v[164:167], v[84:87]
	v_mfma_f32_16x16x32_bf16 v[88:91], v[180:183], v[168:171], v[88:91]
	v_mfma_f32_16x16x32_bf16 v[92:95], v[180:183], v[172:175], v[92:95]
	v_mfma_f32_16x16x32_bf16 v[96:99], v[184:187], v[160:163], v[96:99]
	v_mfma_f32_16x16x32_bf16 v[100:103], v[184:187], v[164:167], v[100:103]
	v_mfma_f32_16x16x32_bf16 v[104:107], v[184:187], v[168:171], v[104:107]
	v_mfma_f32_16x16x32_bf16 v[108:111], v[184:187], v[172:175], v[108:111]
	v_mfma_f32_16x16x32_bf16 v[112:115], v[188:191], v[160:163], v[112:115]
	v_mfma_f32_16x16x32_bf16 v[116:119], v[188:191], v[164:167], v[116:119]
	v_mfma_f32_16x16x32_bf16 v[120:123], v[188:191], v[168:171], v[120:123]
	v_mfma_f32_16x16x32_bf16 v[124:127], v[188:191], v[172:175], v[124:127]
	v_mfma_f32_16x16x32_bf16 v[128:131], v[192:195], v[160:163], v[128:131]
	v_mfma_f32_16x16x32_bf16 v[132:135], v[192:195], v[164:167], v[132:135]
	v_mfma_f32_16x16x32_bf16 v[136:139], v[192:195], v[168:171], v[136:139]
	v_mfma_f32_16x16x32_bf16 v[140:143], v[192:195], v[172:175], v[140:143]
	v_mfma_f32_16x16x32_bf16 v[144:147], v[196:199], v[160:163], v[144:147]
	v_mfma_f32_16x16x32_bf16 v[148:151], v[196:199], v[164:167], v[148:151]
	v_mfma_f32_16x16x32_bf16 v[152:155], v[196:199], v[168:171], v[152:155]
	v_mfma_f32_16x16x32_bf16 v[156:159], v[196:199], v[172:175], v[156:159]
	s_waitcnt vmcnt(0) lgkmcnt(0)
	s_barrier
	v_add_u32_e32 v10, s21, v8
	v_add_u32_e32 v12, s21, v9
	v_xor_b32_e32 v11, 64, v10
	v_xor_b32_e32 v13, 64, v12
	s_add_u32 s21, s21, 0xa000
	s_cmp_ge_u32 s21, 0x1e000
	s_cbranch_scc0 .Ldn_ring_6
	s_sub_u32 s21, s21, 0x1e000
.Ldn_ring_6:
	v_mfma_f32_16x16x32_bf16 v[64:67], v[216:219], v[200:203], v[64:67]
	v_mfma_f32_16x16x32_bf16 v[68:71], v[216:219], v[204:207], v[68:71]
	ds_read_b128 v[160:163], v10 offset:0
	v_mfma_f32_16x16x32_bf16 v[72:75], v[216:219], v[208:211], v[72:75]
	v_mfma_f32_16x16x32_bf16 v[76:79], v[216:219], v[212:215], v[76:79]
	ds_read_b128 v[164:167], v10 offset:2048
	v_mfma_f32_16x16x32_bf16 v[80:83], v[220:223], v[200:203], v[80:83]
	v_mfma_f32_16x16x32_bf16 v[84:87], v[220:223], v[204:207], v[84:87]
	ds_read_b128 v[168:171], v10 offset:4096
	v_mfma_f32_16x16x32_bf16 v[88:91], v[220:223], v[208:211], v[88:91]
	v_mfma_f32_16x16x32_bf16 v[92:95], v[220:223], v[212:215], v[92:95]
	ds_read_b128 v[172:175], v10 offset:6144
	v_mfma_f32_16x16x32_bf16 v[96:99], v[224:227], v[200:203], v[96:99]
	v_mfma_f32_16x16x32_bf16 v[100:103], v[224:227], v[204:207], v[100:103]
	ds_read_b128 v[176:179], v12 offset:0
	v_mfma_f32_16x16x32_bf16 v[104:107], v[224:227], v[208:211], v[104:107]
	v_mfma_f32_16x16x32_bf16 v[108:111], v[224:227], v[212:215], v[108:111]
	ds_read_b128 v[180:183], v12 offset:2048
	v_mfma_f32_16x16x32_bf16 v[112:115], v[228:231], v[200:203], v[112:115]
	v_mfma_f32_16x16x32_bf16 v[116:119], v[228:231], v[204:207], v[116:119]
	ds_read_b128 v[184:187], v12 offset:4096
	v_mfma_f32_16x16x32_bf16 v[120:123], v[228:231], v[208:211], v[120:123]
	v_mfma_f32_16x16x32_bf16 v[124:127], v[228:231], v[212:215], v[124:127]
	ds_read_b128 v[188:191], v12 offset:6144
	v_mfma_f32_16x16x32_bf16 v[128:131], v[232:235], v[200:203], v[128:131]
	v_mfma_f32_16x16x32_bf16 v[132:135], v[232:235], v[204:207], v[132:135]
	ds_read_b128 v[192:195], v12 offset:8192
	v_mfma_f32_16x16x32_bf16 v[136:139], v[232:235], v[208:211], v[136:139]
	v_mfma_f32_16x16x32_bf16 v[140:143], v[232:235], v[212:215], v[140:143]
	ds_read_b128 v[196:199], v12 offset:10240
	v_mfma_f32_16x16x32_bf16 v[144:147], v[236:239], v[200:203], v[144:147]
	v_mfma_f32_16x16x32_bf16 v[148:151], v[236:239], v[204:207], v[148:151]
	global_load_dwordx4 v[16:19], v56, s[8:9] offset:0
	v_mfma_f32_16x16x32_bf16 v[152:155], v[236:239], v[208:211], v[152:155]
	v_mfma_f32_16x16x32_bf16 v[156:159], v[236:239], v[212:215], v[156:159]
	global_load_dwordx4 v[20:23], v57, s[8:9] offset:0
	global_load_dwordx4 v[24:27], v58, s[8:9] offset:0
	global_load_dwordx4 v[28:31], v59, s[8:9] offset:0
	global_load_dwordx4 v[32:35], v56, s[8:9] offset:64
	global_load_dwordx4 v[36:39], v57, s[8:9] offset:64
	global_load_dwordx4 v[40:43], v58, s[8:9] offset:64
	global_load_dwordx4 v[44:47], v59, s[8:9] offset:64
	global_load_dwordx4 v[48:51], v56, s[8:9] offset:128
	global_load_dwordx4 v[52:55], v57, s[8:9] offset:128
	global_load_dwordx4 v[240:243], v58, s[8:9] offset:128
	global_load_dwordx4 v[244:247], v59, s[8:9] offset:128
	global_load_dwordx4 v[248:251], v56, s[8:9] offset:192
	global_load_dwordx4 v[252:255], v57, s[8:9] offset:192
	ds_read_b128 v[200:203], v11 offset:0
	ds_read_b128 v[204:207], v11 offset:2048
	ds_read_b128 v[208:211], v11 offset:4096
	ds_read_b128 v[212:215], v11 offset:6144
	ds_read_b128 v[216:219], v13 offset:0
	ds_read_b128 v[220:223], v13 offset:2048
	ds_read_b128 v[224:227], v13 offset:4096
	ds_read_b128 v[228:231], v13 offset:6144
	ds_read_b128 v[232:235], v13 offset:8192
	ds_read_b128 v[236:239], v13 offset:10240
	s_waitcnt lgkmcnt(10)
	v_mfma_f32_16x16x32_bf16 v[64:67], v[176:179], v[160:163], v[64:67]
	v_mfma_f32_16x16x32_bf16 v[68:71], v[176:179], v[164:167], v[68:71]
	v_mfma_f32_16x16x32_bf16 v[72:75], v[176:179], v[168:171], v[72:75]
	v_mfma_f32_16x16x32_bf16 v[76:79], v[176:179], v[172:175], v[76:79]
	v_mfma_f32_16x16x32_bf16 v[80:83], v[180:183], v[160:163], v[80:83]
	v_mfma_f32_16x16x32_bf16 v[84:87], v[180:183], v[164:167], v[84:87]
	v_mfma_f32_16x16x32_bf16 v[88:91], v[180:183], v[168:171], v[88:91]
	v_mfma_f32_16x16x32_bf16 v[92:95], v[180:183], v[172:175], v[92:95]
	v_mfma_f32_16x16x32_bf16 v[96:99], v[184:187], v[160:163], v[96:99]
	v_mfma_f32_16x16x32_bf16 v[100:103], v[184:187], v[164:167], v[100:103]
	v_mfma_f32_16x16x32_bf16 v[104:107], v[184:187], v[168:171], v[104:107]
	v_mfma_f32_16x16x32_bf16 v[108:111], v[184:187], v[172:175], v[108:111]
	v_mfma_f32_16x16x32_bf16 v[112:115], v[188:191], v[160:163], v[112:115]
	v_mfma_f32_16x16x32_bf16 v[116:119], v[188:191], v[164:167], v[116:119]
	v_mfma_f32_16x16x32_bf16 v[120:123], v[188:191], v[168:171], v[120:123]
	v_mfma_f32_16x16x32_bf16 v[124:127], v[188:191], v[172:175], v[124:127]
	v_mfma_f32_16x16x32_bf16 v[128:131], v[192:195], v[160:163], v[128:131]
	v_mfma_f32_16x16x32_bf16 v[132:135], v[192:195], v[164:167], v[132:135]
	v_mfma_f32_16x16x32_bf16 v[136:139], v[192:195], v[168:171], v[136:139]
	v_mfma_f32_16x16x32_bf16 v[140:143], v[192:195], v[172:175], v[140:143]
	v_mfma_f32_16x16x32_bf16 v[144:147], v[196:199], v[160:163], v[144:147]
	v_mfma_f32_16x16x32_bf16 v[148:151], v[196:199], v[164:167], v[148:151]
	v_mfma_f32_16x16x32_bf16 v[152:155], v[196:199], v[168:171], v[152:155]
	v_mfma_f32_16x16x32_bf16 v[156:159], v[196:199], v[172:175], v[156:159]
	s_waitcnt lgkmcnt(0)
	v_mfma_f32_16x16x32_bf16 v[64:67], v[216:219], v[200:203], v[64:67]
	v_mfma_f32_16x16x32_bf16 v[68:71], v[216:219], v[204:207], v[68:71]
	global_load_dwordx4 v[160:163], v58, s[8:9] offset:192
	v_mfma_f32_16x16x32_bf16 v[72:75], v[216:219], v[208:211], v[72:75]
	v_mfma_f32_16x16x32_bf16 v[76:79], v[216:219], v[212:215], v[76:79]
	global_load_dwordx4 v[164:167], v59, s[8:9] offset:192
	v_mfma_f32_16x16x32_bf16 v[80:83], v[220:223], v[200:203], v[80:83]
	v_mfma_f32_16x16x32_bf16 v[84:87], v[220:223], v[204:207], v[84:87]
	global_load_dwordx4 v[168:171], v56, s[8:9] offset:256
	v_mfma_f32_16x16x32_bf16 v[88:91], v[220:223], v[208:211], v[88:91]
	v_mfma_f32_16x16x32_bf16 v[92:95], v[220:223], v[212:215], v[92:95]
	global_load_dwordx4 v[172:175], v57, s[8:9] offset:256
	v_mfma_f32_16x16x32_bf16 v[96:99], v[224:227], v[200:203], v[96:99]
	v_mfma_f32_16x16x32_bf16 v[100:103], v[224:227], v[204:207], v[100:103]
	global_load_dwordx4 v[176:179], v58, s[8:9] offset:256
	v_mfma_f32_16x16x32_bf16 v[104:107], v[224:227], v[208:211], v[104:107]
	v_mfma_f32_16x16x32_bf16 v[108:111], v[224:227], v[212:215], v[108:111]
	global_load_dwordx4 v[180:183], v59, s[8:9] offset:256
	v_mfma_f32_16x16x32_bf16 v[112:115], v[228:231], v[200:203], v[112:115]
	v_mfma_f32_16x16x32_bf16 v[116:119], v[228:231], v[204:207], v[116:119]
	global_load_dwordx4 v[184:187], v56, s[8:9] offset:320
	v_mfma_f32_16x16x32_bf16 v[120:123], v[228:231], v[208:211], v[120:123]
	v_mfma_f32_16x16x32_bf16 v[124:127], v[228:231], v[212:215], v[124:127]
	global_load_dwordx4 v[188:191], v57, s[8:9] offset:320
	v_mfma_f32_16x16x32_bf16 v[128:131], v[232:235], v[200:203], v[128:131]
	v_mfma_f32_16x16x32_bf16 v[132:135], v[232:235], v[204:207], v[132:135]
	global_load_dwordx4 v[192:195], v58, s[8:9] offset:320
	v_mfma_f32_16x16x32_bf16 v[136:139], v[232:235], v[208:211], v[136:139]
	v_mfma_f32_16x16x32_bf16 v[140:143], v[232:235], v[212:215], v[140:143]
	global_load_dwordx4 v[196:199], v59, s[8:9] offset:320
	v_mfma_f32_16x16x32_bf16 v[144:147], v[236:239], v[200:203], v[144:147]
	v_mfma_f32_16x16x32_bf16 v[148:151], v[236:239], v[204:207], v[148:151]
	v_mfma_f32_16x16x32_bf16 v[152:155], v[236:239], v[208:211], v[152:155]
	v_mfma_f32_16x16x32_bf16 v[156:159], v[236:239], v[212:215], v[156:159]
	s_waitcnt vmcnt(23)
	v_pk_add_f32 v[64:65], v[64:65], v[16:17]
	v_pk_add_f32 v[66:67], v[66:67], v[18:19]
	global_store_dwordx4 v56, v[64:67], s[10:11] offset:0
	s_waitcnt vmcnt(23)
	v_pk_add_f32 v[68:69], v[68:69], v[20:21]
	v_pk_add_f32 v[70:71], v[70:71], v[22:23]
	global_store_dwordx4 v57, v[68:71], s[10:11] offset:0
	s_waitcnt vmcnt(23)
	v_pk_add_f32 v[72:73], v[72:73], v[24:25]
	v_pk_add_f32 v[74:75], v[74:75], v[26:27]
	global_store_dwordx4 v58, v[72:75], s[10:11] offset:0
	s_waitcnt vmcnt(23)
	v_pk_add_f32 v[76:77], v[76:77], v[28:29]
	v_pk_add_f32 v[78:79], v[78:79], v[30:31]
	global_store_dwordx4 v59, v[76:79], s[10:11] offset:0
	s_waitcnt vmcnt(23)
	v_pk_add_f32 v[80:81], v[80:81], v[32:33]
	v_pk_add_f32 v[82:83], v[82:83], v[34:35]
	global_store_dwordx4 v56, v[80:83], s[10:11] offset:64
	s_waitcnt vmcnt(23)
	v_pk_add_f32 v[84:85], v[84:85], v[36:37]
	v_pk_add_f32 v[86:87], v[86:87], v[38:39]
	global_store_dwordx4 v57, v[84:87], s[10:11] offset:64
	s_waitcnt vmcnt(23)
	v_pk_add_f32 v[88:89], v[88:89], v[40:41]
	v_pk_add_f32 v[90:91], v[90:91], v[42:43]
	global_store_dwordx4 v58, v[88:91], s[10:11] offset:64
	s_waitcnt vmcnt(23)
	v_pk_add_f32 v[92:93], v[92:93], v[44:45]
	v_pk_add_f32 v[94:95], v[94:95], v[46:47]
	global_store_dwordx4 v59, v[92:95], s[10:11] offset:64
	s_waitcnt vmcnt(23)
	v_pk_add_f32 v[96:97], v[96:97], v[48:49]
	v_pk_add_f32 v[98:99], v[98:99], v[50:51]
	global_store_dwordx4 v56, v[96:99], s[10:11] offset:128
	s_waitcnt vmcnt(23)
	v_pk_add_f32 v[100:101], v[100:101], v[52:53]
	v_pk_add_f32 v[102:103], v[102:103], v[54:55]
	global_store_dwordx4 v57, v[100:103], s[10:11] offset:128
	s_waitcnt vmcnt(23)
	v_pk_add_f32 v[104:105], v[104:105], v[240:241]
	v_pk_add_f32 v[106:107], v[106:107], v[242:243]
	global_store_dwordx4 v58, v[104:107], s[10:11] offset:128
	s_waitcnt vmcnt(23)
	v_pk_add_f32 v[108:109], v[108:109], v[244:245]
	v_pk_add_f32 v[110:111], v[110:111], v[246:247]
	global_store_dwordx4 v59, v[108:111], s[10:11] offset:128
	s_waitcnt vmcnt(23)
	v_pk_add_f32 v[112:113], v[112:113], v[248:249]
	v_pk_add_f32 v[114:115], v[114:115], v[250:251]
	global_store_dwordx4 v56, v[112:115], s[10:11] offset:192
	s_waitcnt vmcnt(23)
	v_pk_add_f32 v[116:117], v[116:117], v[252:253]
	v_pk_add_f32 v[118:119], v[118:119], v[254:255]
	global_store_dwordx4 v57, v[116:119], s[10:11] offset:192
	s_waitcnt vmcnt(23)
	v_pk_add_f32 v[120:121], v[120:121], v[160:161]
	v_pk_add_f32 v[122:123], v[122:123], v[162:163]
	global_store_dwordx4 v58, v[120:123], s[10:11] offset:192
	s_waitcnt vmcnt(23)
	v_pk_add_f32 v[124:125], v[124:125], v[164:165]
	v_pk_add_f32 v[126:127], v[126:127], v[166:167]
	global_store_dwordx4 v59, v[124:127], s[10:11] offset:192
	s_waitcnt vmcnt(23)
	v_pk_add_f32 v[128:129], v[128:129], v[168:169]
	v_pk_add_f32 v[130:131], v[130:131], v[170:171]
	global_store_dwordx4 v56, v[128:131], s[10:11] offset:256
	s_waitcnt vmcnt(23)
	v_pk_add_f32 v[132:133], v[132:133], v[172:173]
	v_pk_add_f32 v[134:135], v[134:135], v[174:175]
	global_store_dwordx4 v57, v[132:135], s[10:11] offset:256
	s_waitcnt vmcnt(23)
	v_pk_add_f32 v[136:137], v[136:137], v[176:177]
	v_pk_add_f32 v[138:139], v[138:139], v[178:179]
	global_store_dwordx4 v58, v[136:139], s[10:11] offset:256
	s_waitcnt vmcnt(23)
	v_pk_add_f32 v[140:141], v[140:141], v[180:181]
	v_pk_add_f32 v[142:143], v[142:143], v[182:183]
	global_store_dwordx4 v59, v[140:143], s[10:11] offset:256
	s_waitcnt vmcnt(23)
	v_pk_add_f32 v[144:145], v[144:145], v[184:185]
	v_pk_add_f32 v[146:147], v[146:147], v[186:187]
	global_store_dwordx4 v56, v[144:147], s[10:11] offset:320
	s_waitcnt vmcnt(23)
	v_pk_add_f32 v[148:149], v[148:149], v[188:189]
	v_pk_add_f32 v[150:151], v[150:151], v[190:191]
	global_store_dwordx4 v57, v[148:151], s[10:11] offset:320
	s_waitcnt vmcnt(23)
	v_pk_add_f32 v[152:153], v[152:153], v[192:193]
	v_pk_add_f32 v[154:155], v[154:155], v[194:195]
	global_store_dwordx4 v58, v[152:155], s[10:11] offset:320
	s_waitcnt vmcnt(23)
	v_pk_add_f32 v[156:157], v[156:157], v[196:197]
	v_pk_add_f32 v[158:159], v[158:159], v[198:199]
	global_store_dwordx4 v59, v[156:159], s[10:11] offset:320

	.amdhsa_kernel _Z7gemm128ILi3ELi96EEv8GemmArgs
		.amdhsa_group_segment_fixed_size 57344
		.amdhsa_private_segment_fixed_size 0
		.amdhsa_kernarg_size 80
		.amdhsa_user_sgpr_count 2
		.amdhsa_user_sgpr_dispatch_ptr 0
		.amdhsa_user_sgpr_queue_ptr 0
		.amdhsa_user_sgpr_kernarg_segment_ptr 1
		.amdhsa_user_sgpr_dispatch_id 0
		.amdhsa_user_sgpr_kernarg_preload_length 0
		.amdhsa_user_sgpr_kernarg_preload_offset 0
		.amdhsa_user_sgpr_private_segment_size 0
		.amdhsa_uses_dynamic_stack 0
		.amdhsa_enable_private_segment 0
		.amdhsa_system_sgpr_workgroup_id_x 1
		.amdhsa_system_sgpr_workgroup_id_y 0
		.amdhsa_system_sgpr_workgroup_id_z 0
		.amdhsa_system_sgpr_workgroup_info 0
		.amdhsa_system_vgpr_workitem_id 0
		.amdhsa_next_free_vgpr 256
		.amdhsa_next_free_sgpr 24
		.amdhsa_accum_offset 256
		.amdhsa_reserve_vcc 1
		.amdhsa_float_round_mode_32 0
		.amdhsa_float_round_mode_16_64 0
		.amdhsa_float_denorm_mode_32 3
		.amdhsa_float_denorm_mode_16_64 3
		.amdhsa_dx10_clamp 1
		.amdhsa_ieee_mode 1
		.amdhsa_fp16_overflow 0
		.amdhsa_tg_split 0
		.amdhsa_exception_fp_ieee_invalid_op 0
		.amdhsa_exception_fp_denorm_src 0
		.amdhsa_exception_fp_ieee_div_zero 0
		.amdhsa_exception_fp_ieee_overflow 0
		.amdhsa_exception_fp_ieee_underflow 0
		.amdhsa_exception_fp_ieee_inexact 0
		.amdhsa_exception_int_div_zero 0
	.end_amdhsa_kernel

.Lfunc_end4:
	.size	_Z7gemm128ILi3ELi96EEv8GemmArgs, .Lfunc_end4-_Z7gemm128ILi3ELi96EEv8GemmArgs
	.set _Z7gemm128ILi3ELi96EEv8GemmArgs.num_vgpr, 256
	.set _Z7gemm128ILi3ELi96EEv8GemmArgs.num_agpr, 0
	.set _Z7gemm128ILi3ELi96EEv8GemmArgs.numbered_sgpr, 24
	.set _Z7gemm128ILi3ELi96EEv8GemmArgs.num_named_barrier, 0
	.set _Z7gemm128ILi3ELi96EEv8GemmArgs.private_seg_size, 0
	.set _Z7gemm128ILi3ELi96EEv8GemmArgs.uses_vcc, 1
	.set _Z7gemm128ILi3ELi96EEv8GemmArgs.uses_flat_scratch, 0
	.set _Z7gemm128ILi3ELi96EEv8GemmArgs.has_dyn_sized_stack, 0
	.set _Z7gemm128ILi3ELi96EEv8GemmArgs.has_recursion, 0
	.set _Z7gemm128ILi3ELi96EEv8GemmArgs.has_indirect_call, 0

amdhsa.kernels:
  - .agpr_count:     0
    .args:
      - .offset:         0
        .size:           136
        .value_kind:     by_value
      - .offset:         136
        .size:           4
        .value_kind:     hidden_block_count_x
      - .offset:         140
        .size:           4
        .value_kind:     hidden_block_count_y
      - .offset:         144
        .size:           4
        .value_kind:     hidden_block_count_z
      - .offset:         148
        .size:           2
        .value_kind:     hidden_group_size_x
      - .offset:         150
        .size:           2
        .value_kind:     hidden_group_size_y
      - .offset:         152
        .size:           2
        .value_kind:     hidden_group_size_z
      - .offset:         154
        .size:           2
        .value_kind:     hidden_remainder_x
      - .offset:         156
        .size:           2
        .value_kind:     hidden_remainder_y
      - .offset:         158
        .size:           2
        .value_kind:     hidden_remainder_z
      - .offset:         176
        .size:           8
        .value_kind:     hidden_global_offset_x
      - .offset:         184
        .size:           8
        .value_kind:     hidden_global_offset_y
      - .offset:         192
        .size:           8
        .value_kind:     hidden_global_offset_z
      - .offset:         200
        .size:           2
        .value_kind:     hidden_grid_dims
    .group_segment_fixed_size: 16640
    .kernarg_segment_align: 8
    .kernarg_segment_size: 392
    .language:       OpenCL C
    .language_version:
      - 2
      - 0
    .max_flat_workgroup_size: 256
    .name:           _Z11prep_kernel8PrepArgs
    .private_segment_fixed_size: 0
    .sgpr_count:     26
    .sgpr_spill_count: 0
    .symbol:         _Z11prep_kernel8PrepArgs.kd
    .uniform_work_group_size: 1
    .uses_dynamic_stack: false
    .vgpr_count:     46
    .vgpr_spill_count: 0
    .wavefront_size: 64
  - .agpr_count:     0
    .args:
      - .offset:         0
        .size:           216
        .value_kind:     by_value
    .group_segment_fixed_size: 0
    .kernarg_segment_align: 8
    .kernarg_segment_size: 216
    .language:       OpenCL C
    .language_version:
      - 2
      - 0
    .max_flat_workgroup_size: 512
    .name:           _Z11attn_kernel8AttnArgs
    .private_segment_fixed_size: 0
    .sgpr_count:     82
    .sgpr_spill_count: 0
    .symbol:         _Z11attn_kernel8AttnArgs.kd
    .uniform_work_group_size: 1
    .uses_dynamic_stack: false
    .vgpr_count:     220
    .vgpr_spill_count: 0
    .wavefront_size: 64
  - .agpr_count:     0
    .args:
      - .offset:         0
        .size:           80
        .value_kind:     by_value
    .group_segment_fixed_size: 0
    .kernarg_segment_align: 8
    .kernarg_segment_size: 80
    .language:       OpenCL C
    .language_version:
      - 2
      - 0
    .max_flat_workgroup_size: 256
    .name:           _Z7gemm128ILi1ELi96EEv8GemmArgs
    .private_segment_fixed_size: 0
    .sgpr_count:     26
    .sgpr_spill_count: 0
    .symbol:         _Z7gemm128ILi1ELi96EEv8GemmArgs.kd
    .uniform_work_group_size: 1
    .uses_dynamic_stack: false
    .vgpr_count:     141
    .vgpr_spill_count: 0
    .wavefront_size: 64
  - .agpr_count:     0
    .args:
      - .offset:         0
        .size:           80
        .value_kind:     by_value
    .group_segment_fixed_size: 0
    .kernarg_segment_align: 8
    .kernarg_segment_size: 80
    .language:       OpenCL C
    .language_version:
      - 2
      - 0
    .max_flat_workgroup_size: 256
    .name:           _Z7gemm128ILi2ELi128EEv8GemmArgs
    .private_segment_fixed_size: 0
    .sgpr_count:     22
    .sgpr_spill_count: 0
    .symbol:         _Z7gemm128ILi2ELi128EEv8GemmArgs.kd
    .uniform_work_group_size: 1
    .uses_dynamic_stack: false
    .vgpr_count:     166
    .vgpr_spill_count: 0
    .wavefront_size: 64
  - .agpr_count:     0
    .args:
      - .offset:         0
        .size:           80
        .value_kind:     by_value
    .group_segment_fixed_size: 57344
    .kernarg_segment_align: 8
    .kernarg_segment_size: 80
    .language:       OpenCL C
    .language_version:
      - 2
      - 0
    .max_flat_workgroup_size: 256
    .name:           _Z7gemm128ILi3ELi96EEv8GemmArgs
    .private_segment_fixed_size: 0
    .sgpr_count:     30
    .sgpr_spill_count: 0
    .symbol:         _Z7gemm128ILi3ELi96EEv8GemmArgs.kd
    .uniform_work_group_size: 1
    .uses_dynamic_stack: false
    .vgpr_count:     256
    .vgpr_spill_count: 0
    .wavefront_size: 64
  - .agpr_count:     0
    .args:
      - .offset:         0
        .size:           32
        .value_kind:     by_value
      - .offset:         32
        .size:           56
        .value_kind:     by_value
    .group_segment_fixed_size: 0
    .kernarg_segment_align: 8
    .kernarg_segment_size: 88
    .language:       OpenCL C
    .language_version:
      - 2
      - 0
    .max_flat_workgroup_size: 512
    .name:           _Z8gemm_bigIN3pg86EpiQKVEEvNS0_4GemmET_
    .private_segment_fixed_size: 0
    .sgpr_count:     58
    .sgpr_spill_count: 0
    .symbol:         _Z8gemm_bigIN3pg86EpiQKVEEvNS0_4GemmET_.kd
    .uniform_work_group_size: 1
    .uses_dynamic_stack: false
    .vgpr_count:     228
    .vgpr_spill_count: 0
    .wavefront_size: 64
  - .agpr_count:     0
    .args:
      - .offset:         0
        .size:           32
        .value_kind:     by_value
      - .offset:         32
        .size:           32
        .value_kind:     by_value
    .group_segment_fixed_size: 0
    .kernarg_segment_align: 8
    .kernarg_segment_size: 64
    .language:       OpenCL C
    .language_version:
      - 2
      - 0
    .max_flat_workgroup_size: 512
    .name:           _Z8gemm_bigIN3pg85EpiUPEEvNS0_4GemmET_
    .private_segment_fixed_size: 0
    .sgpr_count:     50
    .sgpr_spill_count: 0
    .symbol:         _Z8gemm_bigIN3pg85EpiUPEEvNS0_4GemmET_.kd
    .uniform_work_group_size: 1
    .uses_dynamic_stack: false
    .vgpr_count:     226
    .vgpr_spill_count: 0
    .wavefront_size: 64
